# baseline (speedup 1.0000x reference)
_Z8out_projPKDF16_S0_PKfPf:
	s_load_dwordx8 s[4:11], s[0:1], 0x0
	s_lshl_b32 s1, s2, 5
	s_lshr_b32 s0, s2, 6
	s_and_b32 s3, s1, 0x7e0
	s_mov_b32 s1, 0
	v_lshrrev_b32_e32 v92, 6, v0
	s_lshl_b64 s[12:13], s[0:1], 14
	v_lshl_or_b32 v2, v92, 11, s12
	v_or_b32_e32 v2, s3, v2
	v_mov_b32_e32 v3, s13
	v_and_b32_e32 v1, 63, v0
	v_lshlrev_b64 v[2:3], 8, v[2:3]
	v_lshlrev_b32_e32 v64, 15, v92
	v_mov_b32_e32 v65, 0
	s_waitcnt lgkmcnt(0)
	v_lshl_add_u64 v[2:3], s[4:5], 0, v[2:3]
	v_lshl_add_u64 v[34:35], s[6:7], 0, v[64:65]
	v_lshlrev_b32_e32 v64, 4, v1
	v_lshl_add_u64 v[18:19], v[2:3], 0, v[64:65]
	s_movk_i32 s4, 0x1000
	v_add_co_u32_e32 v36, vcc, s4, v18
	global_load_dwordx4 v[2:5], v[18:19], off
	global_load_dwordx4 v[6:9], v[18:19], off offset:1024
	v_addc_co_u32_e32 v37, vcc, 0, v19, vcc
	global_load_dwordx4 v[10:13], v[18:19], off offset:3072
	global_load_dwordx4 v[14:17], v[18:19], off offset:2048
	s_nop 0
	global_load_dwordx4 v[18:21], v[36:37], off
	global_load_dwordx4 v[22:25], v[36:37], off offset:1024
	global_load_dwordx4 v[26:29], v[36:37], off offset:2048
	global_load_dwordx4 v[30:33], v[36:37], off offset:3072
	s_lshl_b32 s4, s2, 9
	s_mov_b32 s5, s1
	s_and_b32 s4, s4, 0x7000
	v_lshl_add_u64 v[66:67], v[34:35], 0, v[64:65]
	v_lshl_add_u64 v[46:47], v[66:67], 0, s[4:5]
	global_load_dwordx4 v[34:37], v[46:47], off
	s_lshr_b32 s4, s2, 3
	s_add_i32 s5, s4, 1
	s_lshl_b32 s6, s5, 12
	s_mov_b32 s7, s1
	s_and_b32 s6, s6, 0x7000
	v_lshl_add_u64 v[72:73], v[66:67], 0, s[6:7]
	global_load_dwordx4 v[38:41], v[72:73], off
	global_load_dwordx4 v[42:45], v[46:47], off offset:1024
	global_load_dwordx4 v[48:51], v[72:73], off offset:1024
	global_load_dwordx4 v[52:55], v[46:47], off offset:2048
	v_or_b32_e32 v60, 64, v1
	v_or_b32_e32 v61, 0xc0, v1
	v_or_b32_e32 v62, 0x140, v1
	v_or_b32_e32 v1, 0x1c0, v1
	v_lshlrev_b32_e32 v56, 4, v60
	v_lshlrev_b32_e32 v57, 4, v61
	v_lshlrev_b32_e32 v58, 4, v62
	v_lshlrev_b32_e32 v59, 4, v1
	v_lshlrev_b32_e32 v64, 4, v0
	s_movk_i32 s6, 0x70
	v_and_b32_e32 v75, 0x700, v56
	v_and_b32_e32 v76, 0xf00, v57
	v_and_b32_e32 v77, 0x1700, v58
	v_and_b32_e32 v78, 0x1f00, v59
	v_and_b32_e32 v63, 0xf0, v64
	global_load_dwordx4 v[56:59], v[72:73], off offset:2048
	v_and_b32_e32 v93, 31, v0
	v_bfe_u32 v94, v0, 5, 1
	v_bitop3_b32 v0, v0, v63, 48 bitop3:0x6c
	v_bitop3_b32 v80, v60, v63, s6 bitop3:0x6c
	v_bitop3_b32 v81, v61, v63, s6 bitop3:0x6c
	v_bitop3_b32 v82, v62, v63, s6 bitop3:0x6c
	v_bitop3_b32 v1, v1, v63, s6 bitop3:0x6c
	global_load_dwordx4 v[60:63], v[46:47], off offset:3072
	global_load_dwordx4 v[68:71], v[72:73], off offset:3072
	s_mov_b32 s17, 0
	s_add_i32 s16, s4, 2
	s_and_b32 s16, s16, 7
	s_lshl_b32 s16, s16, 12
	v_lshl_add_u64 v[84:85], v[66:67], 0, s[16:17]
	global_load_dwordx4 v[96:99], v[84:85], off
	global_load_dwordx4 v[100:103], v[84:85], off offset:1024
	global_load_dwordx4 v[104:107], v[84:85], off offset:2048
	global_load_dwordx4 v[108:111], v[84:85], off offset:3072
	s_add_i32 s16, s4, 3
	s_and_b32 s16, s16, 7
	s_lshl_b32 s16, s16, 12
	v_lshl_add_u64 v[88:89], v[66:67], 0, s[16:17]
	global_load_dwordx4 v[112:115], v[88:89], off
	global_load_dwordx4 v[116:119], v[88:89], off offset:1024
	global_load_dwordx4 v[120:123], v[88:89], off offset:2048
	global_load_dwordx4 v[124:127], v[88:89], off offset:3072
	s_add_i32 s16, s4, 4
	s_and_b32 s16, s16, 7
	s_lshl_b32 s16, s16, 12
	v_lshl_add_u64 v[84:85], v[66:67], 0, s[16:17]
	global_load_dwordx4 v[128:131], v[84:85], off
	global_load_dwordx4 v[132:135], v[84:85], off offset:1024
	global_load_dwordx4 v[136:139], v[84:85], off offset:2048
	global_load_dwordx4 v[140:143], v[84:85], off offset:3072
	s_add_i32 s16, s4, 5
	s_and_b32 s16, s16, 7
	s_lshl_b32 s16, s16, 12
	v_lshl_add_u64 v[88:89], v[66:67], 0, s[16:17]
	global_load_dwordx4 v[144:147], v[88:89], off
	global_load_dwordx4 v[148:151], v[88:89], off offset:1024
	global_load_dwordx4 v[152:155], v[88:89], off offset:2048
	global_load_dwordx4 v[156:159], v[88:89], off offset:3072
	s_add_i32 s16, s4, 6
	s_and_b32 s16, s16, 7
	s_lshl_b32 s16, s16, 12
	v_lshl_add_u64 v[84:85], v[66:67], 0, s[16:17]
	global_load_dwordx4 v[160:163], v[84:85], off
	global_load_dwordx4 v[164:167], v[84:85], off offset:1024
	global_load_dwordx4 v[168:171], v[84:85], off offset:2048
	global_load_dwordx4 v[172:175], v[84:85], off offset:3072
	s_add_i32 s16, s4, 7
	s_and_b32 s16, s16, 7
	s_lshl_b32 s16, s16, 12
	v_lshl_add_u64 v[88:89], v[66:67], 0, s[16:17]
	global_load_dwordx4 v[176:179], v[88:89], off
	global_load_dwordx4 v[180:183], v[88:89], off offset:1024
	global_load_dwordx4 v[184:187], v[88:89], off offset:2048
	global_load_dwordx4 v[188:191], v[88:89], off offset:3072
	v_lshl_add_u32 v74, v92, 13, 0
	v_and_b32_e32 v79, 0x300, v64
	s_lshl_b32 s6, s2, 2
	v_add3_u32 v0, v74, v79, v0
	v_lshlrev_b32_e32 v86, 4, v94
	s_and_b32 s6, s6, 0xe0
	v_add3_u32 v46, v74, v75, v80
	v_add3_u32 v47, v74, v76, v81
	v_add3_u32 v72, v74, v77, v82
	v_add3_u32 v1, v74, v78, v1
	v_and_b32_e32 v87, 0x70, v64
	v_lshl_add_u32 v95, v93, 8, v74
	s_lshl_b32 s5, s5, 5
	s_and_b32 s5, s5, 0xe0
	s_bfe_u32 s2, s2, 0x30003
	s_xor_b32 s2, s2, 4
	s_waitcnt vmcnt(39)
	ds_write_b128 v0, v[2:5]
	s_waitcnt vmcnt(38)
	ds_write_b128 v46, v[6:9]
	s_waitcnt vmcnt(37)
	ds_write_b128 v47, v[10:13]
	s_waitcnt vmcnt(36)
	ds_write_b128 v0, v[14:17] offset:2048
	s_waitcnt vmcnt(35)
	ds_write_b128 v0, v[18:21] offset:4096
	s_waitcnt vmcnt(34)
	ds_write_b128 v72, v[22:25]
	s_waitcnt vmcnt(33)
	ds_write_b128 v0, v[26:29] offset:6144
	s_waitcnt vmcnt(32)
	ds_write_b128 v1, v[30:33]
	v_or_b32_e32 v0, s6, v86
	v_xad_u32 v0, v0, v87, v95
	s_waitcnt lgkmcnt(0)
	s_barrier
	s_add_i32 s14, s4, 0
	s_and_b32 s14, s14, 7
	v_lshl_or_b32 v76, s14, 5, v86
	v_xad_u32 v76, v76, v87, v95
	ds_read_b128 v[2:5], v76
	s_add_i32 s14, s4, 1
	s_and_b32 s14, s14, 7
	v_lshl_or_b32 v77, s14, 5, v86
	v_xad_u32 v77, v77, v87, v95
	ds_read_b128 v[6:9], v77
	s_add_i32 s14, s4, 2
	s_and_b32 s14, s14, 7
	v_lshl_or_b32 v78, s14, 5, v86
	v_xad_u32 v78, v78, v87, v95
	ds_read_b128 v[10:13], v78
	s_add_i32 s14, s4, 3
	s_and_b32 s14, s14, 7
	v_lshl_or_b32 v79, s14, 5, v86
	v_xad_u32 v79, v79, v87, v95
	ds_read_b128 v[14:17], v79
	s_add_i32 s14, s4, 4
	s_and_b32 s14, s14, 7
	v_lshl_or_b32 v80, s14, 5, v86
	v_xad_u32 v80, v80, v87, v95
	ds_read_b128 v[18:21], v80
	s_add_i32 s14, s4, 5
	s_and_b32 s14, s14, 7
	v_lshl_or_b32 v81, s14, 5, v86
	v_xad_u32 v81, v81, v87, v95
	ds_read_b128 v[22:25], v81
	s_add_i32 s14, s4, 6
	s_and_b32 s14, s14, 7
	v_lshl_or_b32 v82, s14, 5, v86
	v_xad_u32 v82, v82, v87, v95
	ds_read_b128 v[26:29], v82
	s_add_i32 s14, s4, 7
	s_and_b32 s14, s14, 7
	v_lshl_or_b32 v83, s14, 5, v86
	v_xad_u32 v83, v83, v87, v95
	ds_read_b128 v[30:33], v83
	s_lshl_b64 s[0:1], s[0:1], 20
	s_add_u32 s0, s10, s0
	s_addc_u32 s1, s11, s1
	s_lshl_b32 s2, s3, 9
	s_add_u32 s0, s0, s2
	s_addc_u32 s1, s1, 0
	v_lshlrev_b32_e32 v75, 11, v94
	v_lshl_add_u32 v74, v92, 14, 0
	v_lshlrev_b32_e32 v88, 2, v93
	v_add3_u32 v74, v74, v75, v88
	s_waitcnt vmcnt(24) lgkmcnt(7)
	v_mfma_f32_32x32x16_f16 v[192:207], v[2:5], v[34:37], 0
	v_mfma_f32_32x32x16_f16 v[208:223], v[2:5], v[42:45], 0
	v_mfma_f32_32x32x16_f16 v[224:239], v[2:5], v[52:55], 0
	v_mfma_f32_32x32x16_f16 v[240:255], v[2:5], v[60:63], 0
	s_waitcnt vmcnt(24) lgkmcnt(6)
	v_mfma_f32_32x32x16_f16 v[192:207], v[6:9], v[38:41], v[192:207]
	v_mfma_f32_32x32x16_f16 v[208:223], v[6:9], v[48:51], v[208:223]
	v_mfma_f32_32x32x16_f16 v[224:239], v[6:9], v[56:59], v[224:239]
	v_mfma_f32_32x32x16_f16 v[240:255], v[6:9], v[68:71], v[240:255]
	s_waitcnt vmcnt(20) lgkmcnt(5)
	v_mfma_f32_32x32x16_f16 v[192:207], v[10:13], v[96:99], v[192:207]
	v_mfma_f32_32x32x16_f16 v[208:223], v[10:13], v[100:103], v[208:223]
	v_mfma_f32_32x32x16_f16 v[224:239], v[10:13], v[104:107], v[224:239]
	v_mfma_f32_32x32x16_f16 v[240:255], v[10:13], v[108:111], v[240:255]
	s_waitcnt vmcnt(16) lgkmcnt(4)
	v_mfma_f32_32x32x16_f16 v[192:207], v[14:17], v[112:115], v[192:207]
	v_mfma_f32_32x32x16_f16 v[208:223], v[14:17], v[116:119], v[208:223]
	v_mfma_f32_32x32x16_f16 v[224:239], v[14:17], v[120:123], v[224:239]
	v_mfma_f32_32x32x16_f16 v[240:255], v[14:17], v[124:127], v[240:255]
	s_waitcnt vmcnt(12) lgkmcnt(3)
	v_mfma_f32_32x32x16_f16 v[192:207], v[18:21], v[128:131], v[192:207]
	v_mfma_f32_32x32x16_f16 v[208:223], v[18:21], v[132:135], v[208:223]
	v_mfma_f32_32x32x16_f16 v[224:239], v[18:21], v[136:139], v[224:239]
	v_mfma_f32_32x32x16_f16 v[240:255], v[18:21], v[140:143], v[240:255]
	s_waitcnt vmcnt(8) lgkmcnt(2)
	v_mfma_f32_32x32x16_f16 v[192:207], v[22:25], v[144:147], v[192:207]
	v_mfma_f32_32x32x16_f16 v[208:223], v[22:25], v[148:151], v[208:223]
	v_mfma_f32_32x32x16_f16 v[224:239], v[22:25], v[152:155], v[224:239]
	v_mfma_f32_32x32x16_f16 v[240:255], v[22:25], v[156:159], v[240:255]
	s_waitcnt vmcnt(4) lgkmcnt(1)
	v_mfma_f32_32x32x16_f16 v[192:207], v[26:29], v[160:163], v[192:207]
	v_mfma_f32_32x32x16_f16 v[208:223], v[26:29], v[164:167], v[208:223]
	v_mfma_f32_32x32x16_f16 v[224:239], v[26:29], v[168:171], v[224:239]
	v_mfma_f32_32x32x16_f16 v[240:255], v[26:29], v[172:175], v[240:255]
	s_waitcnt vmcnt(0) lgkmcnt(0)
	v_mfma_f32_32x32x16_f16 v[192:207], v[30:33], v[176:179], v[192:207]
	v_mfma_f32_32x32x16_f16 v[208:223], v[30:33], v[180:183], v[208:223]
	v_mfma_f32_32x32x16_f16 v[224:239], v[30:33], v[184:187], v[224:239]
	v_mfma_f32_32x32x16_f16 v[240:255], v[30:33], v[188:191], v[240:255]
	v_add_u32_e32 v77, 0x400, v74
	v_add_u32_e32 v78, 0x1000, v74
	v_add_u32_e32 v79, 0x1400, v74
	v_add_u32_e32 v80, 0x2000, v74
	v_add_u32_e32 v81, 0x2400, v74
	v_add_u32_e32 v82, 0x3000, v74
	v_add_u32_e32 v83, 0x3400, v74
	s_barrier
	s_nop 15
	ds_write2_b32 v74, v192, v208 offset0:0 offset1:32
	ds_write2_b32 v74, v224, v240 offset0:64 offset1:96
	ds_write2_b32 v74, v193, v209 offset0:128 offset1:160
	ds_write2_b32 v74, v225, v241 offset0:192 offset1:224
	ds_write2_b32 v77, v194, v210 offset0:0 offset1:32
	ds_write2_b32 v77, v226, v242 offset0:64 offset1:96
	ds_write2_b32 v77, v195, v211 offset0:128 offset1:160
	ds_write2_b32 v77, v227, v243 offset0:192 offset1:224
	ds_write2_b32 v78, v196, v212 offset0:0 offset1:32
	ds_write2_b32 v78, v228, v244 offset0:64 offset1:96
	ds_write2_b32 v78, v197, v213 offset0:128 offset1:160
	ds_write2_b32 v78, v229, v245 offset0:192 offset1:224
	ds_write2_b32 v79, v198, v214 offset0:0 offset1:32
	ds_write2_b32 v79, v230, v246 offset0:64 offset1:96
	ds_write2_b32 v79, v199, v215 offset0:128 offset1:160
	ds_write2_b32 v79, v231, v247 offset0:192 offset1:224
	ds_write2_b32 v80, v200, v216 offset0:0 offset1:32
	ds_write2_b32 v80, v232, v248 offset0:64 offset1:96
	ds_write2_b32 v80, v201, v217 offset0:128 offset1:160
	ds_write2_b32 v80, v233, v249 offset0:192 offset1:224
	ds_write2_b32 v81, v202, v218 offset0:0 offset1:32
	ds_write2_b32 v81, v234, v250 offset0:64 offset1:96
	ds_write2_b32 v81, v203, v219 offset0:128 offset1:160
	ds_write2_b32 v81, v235, v251 offset0:192 offset1:224
	ds_write2_b32 v82, v204, v220 offset0:0 offset1:32
	ds_write2_b32 v82, v236, v252 offset0:64 offset1:96
	ds_write2_b32 v82, v205, v221 offset0:128 offset1:160
	ds_write2_b32 v82, v237, v253 offset0:192 offset1:224
	ds_write2_b32 v83, v206, v222 offset0:0 offset1:32
	ds_write2_b32 v83, v238, v254 offset0:64 offset1:96
	ds_write2_b32 v83, v207, v223 offset0:128 offset1:160
	ds_write2_b32 v83, v239, v255 offset0:192 offset1:224
	v_and_b32_e32 v0, 0x1f0, v64
	s_waitcnt lgkmcnt(0)
	s_barrier
	global_load_dwordx4 v[0:3], v0, s[8:9]
	v_add_u32_e32 v54, 0, v64
	v_add_u32_e32 v4, 0x10000, v54
	v_add_u32_e32 v8, 0x14000, v54
	v_add_u32_e32 v12, 0x18000, v54
	v_add_u32_e32 v16, 0x1c000, v54
	ds_read_b128 v[4:7], v4
	ds_read_b128 v[8:11], v8
	ds_read_b128 v[12:15], v12
	ds_read_b128 v[16:19], v16
	ds_read_b128 v[20:23], v54
	ds_read_b128 v[24:27], v54 offset:8192
	ds_read_b128 v[28:31], v54 offset:16384
	ds_read_b128 v[32:35], v54 offset:24576
	ds_read_b128 v[36:39], v54 offset:32768
	ds_read_b128 v[40:43], v54 offset:40960
	ds_read_b128 v[44:47], v54 offset:49152
	ds_read_b128 v[48:51], v54 offset:57344
	v_lshl_add_u64 v[52:53], s[0:1], 0, v[64:65]
	s_waitcnt vmcnt(0) lgkmcnt(7)
	v_pk_add_f32 v[22:23], v[2:3], v[22:23]
	v_pk_add_f32 v[20:21], v[0:1], v[20:21]
	s_waitcnt lgkmcnt(6)
	v_pk_add_f32 v[2:3], v[2:3], v[26:27]
	v_pk_add_f32 v[0:1], v[0:1], v[24:25]
	s_waitcnt lgkmcnt(5)
	v_pk_add_f32 v[22:23], v[22:23], v[30:31]
	v_pk_add_f32 v[20:21], v[20:21], v[28:29]
	s_waitcnt lgkmcnt(4)
	v_pk_add_f32 v[2:3], v[2:3], v[34:35]
	v_pk_add_f32 v[24:25], v[0:1], v[32:33]
	s_waitcnt lgkmcnt(3)
	v_pk_add_f32 v[0:1], v[22:23], v[38:39]
	v_pk_add_f32 v[20:21], v[20:21], v[36:37]
	s_waitcnt lgkmcnt(2)
	v_pk_add_f32 v[22:23], v[2:3], v[42:43]
	s_waitcnt lgkmcnt(1)
	v_pk_add_f32 v[0:1], v[0:1], v[46:47]
	v_pk_add_f32 v[2:3], v[20:21], v[44:45]
	v_pk_add_f32 v[0:1], v[0:1], v[6:7]
	v_pk_add_f32 v[2:3], v[2:3], v[4:5]
	v_pk_add_f32 v[0:1], v[0:1], v[10:11]
	v_pk_add_f32 v[2:3], v[2:3], v[8:9]
	v_pk_add_f32 v[0:1], v[0:1], v[14:15]
	v_pk_add_f32 v[4:5], v[2:3], v[12:13]
	v_pk_add_f32 v[2:3], v[0:1], v[18:19]
	v_pk_add_f32 v[0:1], v[4:5], v[16:17]
	global_store_dwordx4 v64, v[0:3], s[0:1] sc1
	v_pk_add_f32 v[4:5], v[24:25], v[40:41]
	s_waitcnt lgkmcnt(0)
	v_pk_add_f32 v[8:9], v[22:23], v[50:51]
	v_add_u32_e32 v0, 0x12000, v54
	ds_read_b128 v[0:3], v0
	v_pk_add_f32 v[10:11], v[4:5], v[48:49]
	v_add_u32_e32 v4, 0x16000, v54
	ds_read_b128 v[4:7], v4
	s_waitcnt lgkmcnt(1)
	v_pk_add_f32 v[14:15], v[10:11], v[0:1]
	v_add_u32_e32 v0, 0x1a000, v54
	v_pk_add_f32 v[12:13], v[8:9], v[2:3]
	ds_read_b128 v[0:3], v0
	v_add_u32_e32 v8, 0x1e000, v54
	ds_read_b128 v[8:11], v8
	s_waitcnt lgkmcnt(2)
	v_pk_add_f32 v[6:7], v[12:13], v[6:7]
	v_pk_add_f32 v[4:5], v[14:15], v[4:5]
	s_waitcnt lgkmcnt(1)
	v_pk_add_f32 v[2:3], v[6:7], v[2:3]
	v_pk_add_f32 v[0:1], v[4:5], v[0:1]
	v_add_co_u32_e32 v4, vcc, 0x2000, v52
	s_waitcnt lgkmcnt(0)
	v_pk_add_f32 v[2:3], v[2:3], v[10:11]
	v_pk_add_f32 v[0:1], v[0:1], v[8:9]
	v_addc_co_u32_e32 v5, vcc, 0, v53, vcc
	global_store_dwordx4 v[4:5], v[0:3], off sc1
	s_endpgm

	.amdhsa_kernel _Z8out_projPKDF16_S0_PKfPf
		.amdhsa_group_segment_fixed_size 0
		.amdhsa_private_segment_fixed_size 0
		.amdhsa_kernarg_size 32
		.amdhsa_user_sgpr_count 2
		.amdhsa_user_sgpr_dispatch_ptr 0
		.amdhsa_user_sgpr_queue_ptr 0
		.amdhsa_user_sgpr_kernarg_segment_ptr 1
		.amdhsa_user_sgpr_dispatch_id 0
		.amdhsa_user_sgpr_kernarg_preload_length 0
		.amdhsa_user_sgpr_kernarg_preload_offset 0
		.amdhsa_user_sgpr_private_segment_size 0
		.amdhsa_uses_dynamic_stack 0
		.amdhsa_enable_private_segment 0
		.amdhsa_system_sgpr_workgroup_id_x 1
		.amdhsa_system_sgpr_workgroup_id_y 0
		.amdhsa_system_sgpr_workgroup_id_z 0
		.amdhsa_system_sgpr_workgroup_info 0
		.amdhsa_system_vgpr_workitem_id 0
		.amdhsa_next_free_vgpr 256
		.amdhsa_next_free_sgpr 18
		.amdhsa_accum_offset 256
		.amdhsa_reserve_vcc 1
		.amdhsa_float_round_mode_32 0
		.amdhsa_float_round_mode_16_64 0
		.amdhsa_float_denorm_mode_32 3
		.amdhsa_float_denorm_mode_16_64 3
		.amdhsa_dx10_clamp 1
		.amdhsa_ieee_mode 1
		.amdhsa_fp16_overflow 0
		.amdhsa_tg_split 0
		.amdhsa_exception_fp_ieee_invalid_op 0
		.amdhsa_exception_fp_denorm_src 0
		.amdhsa_exception_fp_ieee_div_zero 0
		.amdhsa_exception_fp_ieee_overflow 0
		.amdhsa_exception_fp_ieee_underflow 0
		.amdhsa_exception_fp_ieee_inexact 0
		.amdhsa_exception_int_div_zero 0
	.end_amdhsa_kernel
